# edge staging loads without the nt hint (plain loads); otherwise as the best version
# speedup vs baseline: 1.1221x; 1.0064x over previous
_Z5k_hopILi0EEvPKiPK15HIP_vector_typeIiLj2EEPKS2_IjLj4EEPS6_S8_S8_PKfSB_Pf:
	s_lshr_b32 s3, s2, 3
	s_cmpk_gt_u32 s3, 156
	s_cbranch_scc1 .Lhq0_exit
	s_load_dwordx4 s[4:7], s[0:1], 0x0
	s_load_dwordx4 s[8:11], s[0:1], 0x10
	v_lshrrev_b32_e32 v2, 6, v0
	v_and_b32_e32 v3, 63, v0
	s_bfe_u32 s13, s2, 0x10002
	s_and_b32 s14, s2, 3
	v_readfirstlane_b32 s12, v2
	s_lshl_b32 s15, s3, 2
	s_add_i32 s15, s15, s12
	s_mul_i32 s15, s15, 40
	s_mul_i32 s16, s14, 25000
	s_add_i32 s15, s15, s16
	s_add_i32 s16, s16, 24960
	s_min_u32 s15, s15, s16
	s_mul_i32 s17, s13, 0x61a84
	s_waitcnt lgkmcnt(0)
	s_add_u32 s4, s4, s17
	s_addc_u32 s5, s5, 0
	s_mul_i32 s17, s13, 0x927c00
	s_add_u32 s6, s6, s17
	s_addc_u32 s7, s7, 0
	s_mul_i32 s17, s13, 0xc35000
	s_add_u32 s8, s8, s17
	s_addc_u32 s9, s9, 0
	s_add_u32 s10, s10, s17
	s_addc_u32 s11, s11, 0
	s_mul_i32 s28, s12, 6976
	s_mov_b32 s29, 0xffff80
	v_min_u32_e32 v4, 40, v3
	v_add_u32_e32 v4, s15, v4
	v_lshlrev_b32_e32 v4, 2, v4
	global_load_dword v5, v4, s[4:5]
	v_and_b32_e32 v1, 7, v0
	v_lshlrev_b32_e32 v1, 4, v1
	v_lshrrev_b32_e32 v2, 3, v3
	v_lshlrev_b32_e32 v2, 2, v2
	v_lshlrev_b32_e32 v4, 3, v3
	v_add_u32_e32 v6, s28, v4
	v_add_u32_e32 v7, 1, v3
	v_lshlrev_b32_e32 v7, 2, v7
	s_waitcnt vmcnt(0)
	v_readlane_b32 s18, v5, 0
	v_readlane_b32 s19, v5, 40
	ds_bpermute_b32 v8, v7, v5
	s_sub_i32 s20, s19, s18
	s_lshl_b32 s21, s18, 3
	s_add_u32 s22, s6, s21
	s_addc_u32 s23, s7, 0
	s_add_u32 s24, s22, 0x1000
	s_addc_u32 s25, s23, 0
	s_cmpk_gt_i32 s20, 832
	s_cbranch_scc1 .Lhq0_staged
	global_load_dwordx2 v[56:57], v4, s[22:23] offset:0
	s_cmpk_le_i32 s20, 64
	s_cbranch_scc1 .Lhq0_staged
	global_load_dwordx2 v[58:59], v4, s[22:23] offset:512
	s_cmpk_le_i32 s20, 128
	s_cbranch_scc1 .Lhq0_staged
	global_load_dwordx2 v[60:61], v4, s[22:23] offset:1024
	s_cmpk_le_i32 s20, 192
	s_cbranch_scc1 .Lhq0_staged
	global_load_dwordx2 v[62:63], v4, s[22:23] offset:1536
	s_cmpk_le_i32 s20, 256
	s_cbranch_scc1 .Lhq0_staged
	global_load_dwordx2 v[64:65], v4, s[22:23] offset:2048
	s_cmpk_le_i32 s20, 320
	s_cbranch_scc1 .Lhq0_staged
	global_load_dwordx2 v[66:67], v4, s[22:23] offset:2560
	s_cmpk_le_i32 s20, 384
	s_cbranch_scc1 .Lhq0_staged
	global_load_dwordx2 v[68:69], v4, s[22:23] offset:3072
	s_cmpk_le_i32 s20, 448
	s_cbranch_scc1 .Lhq0_staged
	global_load_dwordx2 v[70:71], v4, s[22:23] offset:3584
	s_cmpk_le_i32 s20, 512
	s_cbranch_scc1 .Lhq0_staged
	global_load_dwordx2 v[72:73], v4, s[24:25] offset:0
	s_cmpk_le_i32 s20, 576
	s_cbranch_scc1 .Lhq0_staged
	global_load_dwordx2 v[74:75], v4, s[24:25] offset:512
	s_cmpk_le_i32 s20, 640
	s_cbranch_scc1 .Lhq0_staged
	global_load_dwordx2 v[76:77], v4, s[24:25] offset:1024
	s_cmpk_le_i32 s20, 704
	s_cbranch_scc1 .Lhq0_staged
	global_load_dwordx2 v[78:79], v4, s[24:25] offset:1536
	s_cmpk_le_i32 s20, 768
	s_cbranch_scc1 .Lhq0_staged
	global_load_dwordx2 v[80:81], v4, s[24:25] offset:2048

.Lhq0_epilogue:
	v_bfe_u32 v2, v0, 3, 3
	v_lshlrev_b32_e32 v2, 2, v2
	v_add_u32_e32 v2, s28, v2
	ds_read_b32 v46, v2 offset:6720
	ds_read_b32 v47, v2 offset:6752
	ds_read_b32 v48, v2 offset:6784
	ds_read_b32 v49, v2 offset:6816
	ds_read_b32 v50, v2 offset:6848
	s_waitcnt lgkmcnt(0)
	v_add_u32_e32 v46, s15, v46
	v_add_u32_e32 v47, s15, v47
	v_add_u32_e32 v48, s15, v48
	v_add_u32_e32 v49, s15, v49
	v_add_u32_e32 v50, s15, v50
	v_lshlrev_b32_e32 v51, 7, v46
	v_or_b32_e32 v51, v51, v1
	v_cvt_pk_f16_f32 v6, v56, v57
	v_cvt_pk_f16_f32 v7, v58, v59
	v_cvt_pk_f16_f32 v8, v60, v61
	v_cvt_pk_f16_f32 v9, v62, v63
	global_store_dwordx4 v51, v[6:9], s[10:11] nt
	v_lshlrev_b32_e32 v52, 7, v47
	v_or_b32_e32 v52, v52, v1
	v_cvt_pk_f16_f32 v10, v64, v65
	v_cvt_pk_f16_f32 v11, v66, v67
	v_cvt_pk_f16_f32 v12, v68, v69
	v_cvt_pk_f16_f32 v13, v70, v71
	global_store_dwordx4 v52, v[10:13], s[10:11] nt
	v_lshlrev_b32_e32 v53, 7, v48
	v_or_b32_e32 v53, v53, v1
	v_cvt_pk_f16_f32 v14, v72, v73
	v_cvt_pk_f16_f32 v15, v74, v75
	v_cvt_pk_f16_f32 v16, v76, v77
	v_cvt_pk_f16_f32 v17, v78, v79
	global_store_dwordx4 v53, v[14:17], s[10:11] nt
	v_lshlrev_b32_e32 v54, 7, v49
	v_or_b32_e32 v54, v54, v1
	v_cvt_pk_f16_f32 v18, v80, v81
	v_cvt_pk_f16_f32 v19, v82, v83
	v_cvt_pk_f16_f32 v20, v84, v85
	v_cvt_pk_f16_f32 v21, v86, v87
	global_store_dwordx4 v54, v[18:21], s[10:11] nt
	v_lshlrev_b32_e32 v55, 7, v50
	v_or_b32_e32 v55, v55, v1
	v_cvt_pk_f16_f32 v22, v88, v89
	v_cvt_pk_f16_f32 v23, v90, v91
	v_cvt_pk_f16_f32 v24, v92, v93
	v_cvt_pk_f16_f32 v25, v94, v95
	global_store_dwordx4 v55, v[22:25], s[10:11] nt

_Z5k_hopILi1EEvPKiPK15HIP_vector_typeIiLj2EEPKS2_IjLj4EEPS6_S8_S8_PKfSB_Pf:
	s_lshr_b32 s3, s2, 3
	s_cmpk_gt_u32 s3, 156
	s_cbranch_scc1 .Lhq1_exit
	s_load_dwordx4 s[4:7], s[0:1], 0x0
	s_load_dwordx4 s[8:11], s[0:1], 0x10
	s_load_dwordx4 s[48:51], s[0:1], 0x20
	s_load_dwordx4 s[52:55], s[0:1], 0x30
	s_load_dwordx2 s[56:57], s[0:1], 0x40
	v_lshrrev_b32_e32 v2, 6, v0
	v_and_b32_e32 v3, 63, v0
	s_bfe_u32 s13, s2, 0x10002
	s_and_b32 s14, s2, 3
	v_readfirstlane_b32 s12, v2
	s_lshl_b32 s15, s3, 2
	s_add_i32 s15, s15, s12
	s_mul_i32 s15, s15, 40
	s_mul_i32 s16, s14, 25000
	s_add_i32 s15, s15, s16
	s_add_i32 s16, s16, 24960
	s_min_u32 s15, s15, s16
	s_mul_i32 s17, s13, 0x61a84
	s_waitcnt lgkmcnt(0)
	s_add_u32 s4, s4, s17
	s_addc_u32 s5, s5, 0
	s_mul_i32 s17, s13, 0x927c00
	s_add_u32 s6, s6, s17
	s_addc_u32 s7, s7, 0
	s_mul_i32 s17, s13, 0xc35000
	s_add_u32 s8, s8, s17
	s_addc_u32 s9, s9, 0
	s_add_u32 s48, s48, s17
	s_addc_u32 s49, s49, 0
	s_add_u32 s50, s50, s17
	s_addc_u32 s51, s51, 0
	s_cmp_eq_u32 s13, 0
	s_cselect_b32 s58, s52, s54
	s_cselect_b32 s59, s53, s55
	s_load_dwordx4 s[52:55], s[58:59], 0x0
	s_lshl_b32 s17, s13, 8
	s_add_u32 s56, s56, s17
	s_addc_u32 s57, s57, 0
	s_mul_i32 s28, s12, 6976
	s_mov_b32 s29, 0xffff80
	v_min_u32_e32 v4, 40, v3
	v_add_u32_e32 v4, s15, v4
	v_lshlrev_b32_e32 v4, 2, v4
	global_load_dword v5, v4, s[4:5]
	v_and_b32_e32 v1, 7, v0
	v_lshlrev_b32_e32 v1, 4, v1
	v_lshrrev_b32_e32 v2, 3, v3
	v_lshlrev_b32_e32 v2, 2, v2
	v_lshlrev_b32_e32 v4, 3, v3
	v_add_u32_e32 v6, s28, v4
	v_add_u32_e32 v7, 1, v3
	v_lshlrev_b32_e32 v7, 2, v7
	s_waitcnt vmcnt(0)
	v_readlane_b32 s18, v5, 0
	v_readlane_b32 s19, v5, 40
	ds_bpermute_b32 v8, v7, v5
	s_sub_i32 s20, s19, s18
	s_lshl_b32 s21, s18, 3
	s_add_u32 s22, s6, s21
	s_addc_u32 s23, s7, 0
	s_add_u32 s24, s22, 0x1000
	s_addc_u32 s25, s23, 0
	s_cmpk_gt_i32 s20, 832
	s_cbranch_scc1 .Lhq1_staged
	global_load_dwordx2 v[56:57], v4, s[22:23] offset:0
	s_cmpk_le_i32 s20, 64
	s_cbranch_scc1 .Lhq1_staged
	global_load_dwordx2 v[58:59], v4, s[22:23] offset:512
	s_cmpk_le_i32 s20, 128
	s_cbranch_scc1 .Lhq1_staged
	global_load_dwordx2 v[60:61], v4, s[22:23] offset:1024
	s_cmpk_le_i32 s20, 192
	s_cbranch_scc1 .Lhq1_staged
	global_load_dwordx2 v[62:63], v4, s[22:23] offset:1536
	s_cmpk_le_i32 s20, 256
	s_cbranch_scc1 .Lhq1_staged
	global_load_dwordx2 v[64:65], v4, s[22:23] offset:2048
	s_cmpk_le_i32 s20, 320
	s_cbranch_scc1 .Lhq1_staged
	global_load_dwordx2 v[66:67], v4, s[22:23] offset:2560
	s_cmpk_le_i32 s20, 384
	s_cbranch_scc1 .Lhq1_staged
	global_load_dwordx2 v[68:69], v4, s[22:23] offset:3072
	s_cmpk_le_i32 s20, 448
	s_cbranch_scc1 .Lhq1_staged
	global_load_dwordx2 v[70:71], v4, s[22:23] offset:3584
	s_cmpk_le_i32 s20, 512
	s_cbranch_scc1 .Lhq1_staged
	global_load_dwordx2 v[72:73], v4, s[24:25] offset:0
	s_cmpk_le_i32 s20, 576
	s_cbranch_scc1 .Lhq1_staged
	global_load_dwordx2 v[74:75], v4, s[24:25] offset:512
	s_cmpk_le_i32 s20, 640
	s_cbranch_scc1 .Lhq1_staged
	global_load_dwordx2 v[76:77], v4, s[24:25] offset:1024
	s_cmpk_le_i32 s20, 704
	s_cbranch_scc1 .Lhq1_staged
	global_load_dwordx2 v[78:79], v4, s[24:25] offset:1536
	s_cmpk_le_i32 s20, 768
	s_cbranch_scc1 .Lhq1_staged
	global_load_dwordx2 v[80:81], v4, s[24:25] offset:2048
